# grid barrier: XCD-last workgroup adds to 16 replicated top counters (one per XCD, own 256-B line); each workgroup polls its own XCD's copy (64 pollers per word instead of 512)
# speedup vs baseline: 1.0066x; 1.0066x over previous
; __device__ __forceinline__ unsigned xb_ld(unsigned* p)              { return __hip_atomic_load(p, __ATOMIC_RELAXED, __HIP_MEMORY_SCOPE_AGENT); }
; __device__ __forceinline__ unsigned xb_add(unsigned* p, unsigned v) { return __hip_atomic_fetch_add(p, v, __ATOMIC_RELAXED, __HIP_MEMORY_SCOPE_AGENT); }
; #define XB_SPIN(cond, bar) do { unsigned _sp = 0; while (cond) { __builtin_amdgcn_s_sleep(1); \
;     if ((++_sp & 255u) == 0u) { if (xb_ld(&(bar)[XB_TMO])) break; if (_sp > XB_SPIN_CAP) { atomicAdd(&(bar)[XB_TMO], 1u); break; } } } } while (0)
; __device__ __forceinline__ void xcd_barrier(const XcdBarrier& b) {
;     ...
;         if (nloc == 0u) { xcd_barrier_complete(bar, b.x, nloc, nx); b.st[0] = nloc; b.st[1] = nx; }
;         const unsigned old = xb_add(&bar[XB_XSUB(b.x)], 1u);
;         const unsigned gen = old / nloc;
;         if (old + 1u == (gen + 1u) * nloc) {
;             __builtin_amdgcn_fence(__ATOMIC_RELEASE, "agent");
;             asm volatile("s_waitcnt vmcnt(0)" ::: "memory");
;             const unsigned og = xb_add(&bar[XB_TOP], 1u);
;             const unsigned tg = og / nx;
;             if (og + 1u == (tg + 1u) * nx) xb_add(&bar[XB_TOPGEN], 1u);
;             else XB_SPIN(xb_ld(&bar[XB_TOPGEN]) == tg, bar);
;             __builtin_amdgcn_fence(__ATOMIC_ACQUIRE, "agent");
;             xb_add(&bar[XB_XGEN(b.x)], 1u);
;             asm volatile("s_waitcnt vmcnt(0)" ::: "memory");
;         } else {
;             XB_SPIN(xb_ld(&bar[XB_XGEN(b.x)]) == gen, bar);
.LBB0_726:
	s_or_b64 exec, exec, s[28:29]
	v_readlane_b32 s16, v252, 40
	v_readlane_b32 s17, v252, 41
	v_readlane_b32 s6, v252, 44
	v_readlane_b32 s7, v252, 45
	v_readlane_b32 s42, v252, 42
	v_readlane_b32 s43, v252, 43
	v_mov_b32_e32 v6, 1
	v_add_u32_e32 v255, 1, v255
	s_nop 2
	global_atomic_add v6, v3, v6, s[16:17] sc0
	v_mul_lo_u32 v7, v255, v4
	v_mul_lo_u32 v5, v255, v2
	s_waitcnt vmcnt(0)
	v_add_u32_e32 v8, 1, v6
	v_cmp_eq_u32_e32 vcc, v7, v8
	s_and_saveexec_b64 s[28:29], vcc
	s_cbranch_execz .Lxb_notlast
	buffer_wbl2 sc1
	s_waitcnt vmcnt(0)
	v_mov_b32_e32 v6, 1
	s_add_u32 s6, s6, 0xfffff000
	s_addc_u32 s7, s7, -1
	global_atomic_add v3, v6, s[6:7] offset:0
	global_atomic_add v3, v6, s[6:7] offset:256
	global_atomic_add v3, v6, s[6:7] offset:512
	global_atomic_add v3, v6, s[6:7] offset:768
	global_atomic_add v3, v6, s[6:7] offset:1024
	global_atomic_add v3, v6, s[6:7] offset:1280
	global_atomic_add v3, v6, s[6:7] offset:1536
	global_atomic_add v3, v6, s[6:7] offset:1792
	global_atomic_add v3, v6, s[6:7] offset:2048
	global_atomic_add v3, v6, s[6:7] offset:2304
	global_atomic_add v3, v6, s[6:7] offset:2560
	global_atomic_add v3, v6, s[6:7] offset:2816
	global_atomic_add v3, v6, s[6:7] offset:3072
	global_atomic_add v3, v6, s[6:7] offset:3328
	global_atomic_add v3, v6, s[6:7] offset:3584
	global_atomic_add v3, v6, s[6:7] offset:3840

; __device__ __forceinline__ unsigned xb_ld(unsigned* p)              { return __hip_atomic_load(p, __ATOMIC_RELAXED, __HIP_MEMORY_SCOPE_AGENT); }
; __device__ __forceinline__ unsigned xb_add(unsigned* p, unsigned v) { return __hip_atomic_fetch_add(p, v, __ATOMIC_RELAXED, __HIP_MEMORY_SCOPE_AGENT); }
; #define XB_SPIN(cond, bar) do { unsigned _sp = 0; while (cond) { __builtin_amdgcn_s_sleep(1); \
;     if ((++_sp & 255u) == 0u) { if (xb_ld(&(bar)[XB_TMO])) break; if (_sp > XB_SPIN_CAP) { atomicAdd(&(bar)[XB_TMO], 1u); break; } } } } while (0)
; __device__ __forceinline__ void xcd_barrier(const XcdBarrier& b) {
;     ...
;             else XB_SPIN(xb_ld(&bar[XB_TOPGEN]) == tg, bar);
;             __builtin_amdgcn_fence(__ATOMIC_ACQUIRE, "agent");
;             xb_add(&bar[XB_XGEN(b.x)], 1u);
;             asm volatile("s_waitcnt vmcnt(0)" ::: "memory");
;         } else {
;             XB_SPIN(xb_ld(&bar[XB_XGEN(b.x)]) == gen, bar);
.Lxb_poll:
	global_load_dword v6, v3, s[42:43] sc1
	s_waitcnt vmcnt(0)
	v_cmp_ge_u32_e32 vcc, v6, v5
	s_cbranch_vccnz .Lxb_done
	s_add_i32 s15, s15, 1
	s_cmp_lt_u32 s15, 0x400000
	s_cbranch_scc0 .Lxb_done
	s_sleep 1
	s_branch .Lxb_poll
